# speedup vs baseline: 1.0279x; 1.0279x over previous
.Lq_noprio:
	s_waitcnt vmcnt(12)
	v_cvt_pk_f16_f32 v164, v36, v40
	v_cvt_pk_f16_f32 v180, v68, v72
	v_pk_add_f16 v164, v164, -0.5 op_sel_hi:[1,0]
	v_pk_add_f16 v180, v180, -0.5 op_sel_hi:[1,0]
	v_pk_mul_f16 v196, v180, v180
	v_pk_mul_f16 v212, v164, v180
	v_pk_fma_f16 v196, v164, v164, v196
	v_cvt_pk_f16_f32 v168, v37, v41
	v_cvt_pk_f16_f32 v184, v69, v73
	v_pk_add_f16 v168, v168, -0.5 op_sel_hi:[1,0]
	v_pk_add_f16 v184, v184, -0.5 op_sel_hi:[1,0]
	v_pk_mul_f16 v200, v184, v184
	v_pk_mul_f16 v216, v168, v184
	v_pk_fma_f16 v200, v168, v168, v200
	v_cvt_pk_f16_f32 v172, v38, v42
	v_cvt_pk_f16_f32 v188, v70, v74
	v_pk_add_f16 v172, v172, -0.5 op_sel_hi:[1,0]
	v_pk_add_f16 v188, v188, -0.5 op_sel_hi:[1,0]
	v_pk_mul_f16 v204, v188, v188
	v_pk_mul_f16 v220, v172, v188
	v_pk_fma_f16 v204, v172, v172, v204
	v_cvt_pk_f16_f32 v176, v39, v43
	v_cvt_pk_f16_f32 v192, v71, v75
	v_pk_add_f16 v176, v176, -0.5 op_sel_hi:[1,0]
	v_pk_add_f16 v192, v192, -0.5 op_sel_hi:[1,0]
	v_pk_mul_f16 v208, v192, v192
	v_pk_mul_f16 v224, v176, v192
	v_pk_fma_f16 v208, v176, v176, v208
	s_waitcnt vmcnt(8)
	v_cvt_pk_f16_f32 v165, v44, v48
	v_cvt_pk_f16_f32 v181, v76, v80
	v_pk_add_f16 v165, v165, -0.5 op_sel_hi:[1,0]
	v_pk_add_f16 v181, v181, -0.5 op_sel_hi:[1,0]
	v_pk_mul_f16 v197, v181, v181
	v_pk_mul_f16 v213, v165, v181
	v_pk_fma_f16 v197, v165, v165, v197
	v_cvt_pk_f16_f32 v169, v45, v49
	v_cvt_pk_f16_f32 v185, v77, v81
	v_pk_add_f16 v169, v169, -0.5 op_sel_hi:[1,0]
	v_pk_add_f16 v185, v185, -0.5 op_sel_hi:[1,0]
	v_pk_mul_f16 v201, v185, v185
	v_pk_mul_f16 v217, v169, v185
	v_pk_fma_f16 v201, v169, v169, v201
	v_cvt_pk_f16_f32 v173, v46, v50
	v_cvt_pk_f16_f32 v189, v78, v82
	v_pk_add_f16 v173, v173, -0.5 op_sel_hi:[1,0]
	v_pk_add_f16 v189, v189, -0.5 op_sel_hi:[1,0]
	v_pk_mul_f16 v205, v189, v189
	v_pk_mul_f16 v221, v173, v189
	v_pk_fma_f16 v205, v173, v173, v205
	v_cvt_pk_f16_f32 v177, v47, v51
	v_cvt_pk_f16_f32 v193, v79, v83
	v_pk_add_f16 v177, v177, -0.5 op_sel_hi:[1,0]
	v_pk_add_f16 v193, v193, -0.5 op_sel_hi:[1,0]
	v_pk_mul_f16 v209, v193, v193
	v_pk_mul_f16 v225, v177, v193
	v_pk_fma_f16 v209, v177, v177, v209
	s_waitcnt vmcnt(4)
	v_cvt_pk_f16_f32 v166, v52, v56
	v_cvt_pk_f16_f32 v182, v84, v88
	v_pk_add_f16 v166, v166, -0.5 op_sel_hi:[1,0]
	v_pk_add_f16 v182, v182, -0.5 op_sel_hi:[1,0]
	v_pk_mul_f16 v198, v182, v182
	v_pk_mul_f16 v214, v166, v182
	v_pk_fma_f16 v198, v166, v166, v198
	v_cvt_pk_f16_f32 v170, v53, v57
	v_cvt_pk_f16_f32 v186, v85, v89
	v_pk_add_f16 v170, v170, -0.5 op_sel_hi:[1,0]
	v_pk_add_f16 v186, v186, -0.5 op_sel_hi:[1,0]
	v_pk_mul_f16 v202, v186, v186
	v_pk_mul_f16 v218, v170, v186
	v_pk_fma_f16 v202, v170, v170, v202
	v_cvt_pk_f16_f32 v174, v54, v58
	v_cvt_pk_f16_f32 v190, v86, v90
	v_pk_add_f16 v174, v174, -0.5 op_sel_hi:[1,0]
	v_pk_add_f16 v190, v190, -0.5 op_sel_hi:[1,0]
	v_pk_mul_f16 v206, v190, v190
	v_pk_mul_f16 v222, v174, v190
	v_pk_fma_f16 v206, v174, v174, v206
	v_cvt_pk_f16_f32 v178, v55, v59
	v_cvt_pk_f16_f32 v194, v87, v91
	v_pk_add_f16 v178, v178, -0.5 op_sel_hi:[1,0]
	v_pk_add_f16 v194, v194, -0.5 op_sel_hi:[1,0]
	v_pk_mul_f16 v210, v194, v194
	v_pk_mul_f16 v226, v178, v194
	v_pk_fma_f16 v210, v178, v178, v210
	s_waitcnt vmcnt(0)
	v_cvt_pk_f16_f32 v167, v60, v64
	v_cvt_pk_f16_f32 v183, v92, v96
	v_pk_add_f16 v167, v167, -0.5 op_sel_hi:[1,0]
	v_pk_add_f16 v183, v183, -0.5 op_sel_hi:[1,0]
	v_pk_mul_f16 v199, v183, v183
	v_pk_mul_f16 v215, v167, v183
	v_pk_fma_f16 v199, v167, v167, v199
	v_cvt_pk_f16_f32 v171, v61, v65
	v_cvt_pk_f16_f32 v187, v93, v97
	v_pk_add_f16 v171, v171, -0.5 op_sel_hi:[1,0]
	v_pk_add_f16 v187, v187, -0.5 op_sel_hi:[1,0]
	v_pk_mul_f16 v203, v187, v187
	v_pk_mul_f16 v219, v171, v187
	v_pk_fma_f16 v203, v171, v171, v203
	v_cvt_pk_f16_f32 v175, v62, v66
	v_cvt_pk_f16_f32 v191, v94, v98
	v_pk_add_f16 v175, v175, -0.5 op_sel_hi:[1,0]
	v_pk_add_f16 v191, v191, -0.5 op_sel_hi:[1,0]
	v_pk_mul_f16 v207, v191, v191
	v_pk_mul_f16 v223, v175, v191
	v_pk_fma_f16 v207, v175, v175, v207
	v_cvt_pk_f16_f32 v179, v63, v67
	v_cvt_pk_f16_f32 v195, v95, v99
	v_pk_add_f16 v179, v179, -0.5 op_sel_hi:[1,0]
	v_pk_add_f16 v195, v195, -0.5 op_sel_hi:[1,0]
	v_pk_mul_f16 v211, v195, v195
	v_pk_mul_f16 v227, v179, v195
	v_pk_fma_f16 v211, v179, v179, v211
	global_load_dwordx4 v[100:103], v240, s[18:19] offset:0 sc1 nt
	global_load_dwordx4 v[104:107], v240, s[18:19] offset:2048 sc1 nt
	global_load_dwordx4 v[132:135], v240, s[20:21] offset:0 sc1 nt
	global_load_dwordx4 v[136:139], v240, s[20:21] offset:2048 sc1 nt
	global_load_dwordx4 v[108:111], v241, s[18:19] offset:0 sc1 nt
	global_load_dwordx4 v[112:115], v241, s[18:19] offset:2048 sc1 nt
	global_load_dwordx4 v[140:143], v241, s[20:21] offset:0 sc1 nt
	global_load_dwordx4 v[144:147], v241, s[20:21] offset:2048 sc1 nt
	global_load_dwordx4 v[116:119], v242, s[18:19] offset:0 sc1 nt
	global_load_dwordx4 v[120:123], v242, s[18:19] offset:2048 sc1 nt
	global_load_dwordx4 v[148:151], v242, s[20:21] offset:0 sc1 nt
	global_load_dwordx4 v[152:155], v242, s[20:21] offset:2048 sc1 nt
	global_load_dwordx4 v[124:127], v243, s[18:19] offset:0 sc1 nt
	global_load_dwordx4 v[128:131], v243, s[18:19] offset:2048 sc1 nt
	global_load_dwordx4 v[156:159], v243, s[20:21] offset:0 sc1 nt
	global_load_dwordx4 v[160:163], v243, s[20:21] offset:2048 sc1 nt
	v_mfma_f32_16x16x32_f16 v[68:71], v[164:167], v[24:27], 0
	v_mfma_f32_16x16x32_f16 v[72:75], v[168:171], v[24:27], 0
	v_mfma_f32_16x16x32_f16 v[76:79], v[172:175], v[24:27], 0
	v_mfma_f32_16x16x32_f16 v[80:83], v[176:179], v[24:27], 0
	v_mfma_f32_16x16x32_f16 v[84:87], v[180:183], v[24:27], 0
	v_mfma_f32_16x16x32_f16 v[88:91], v[184:187], v[24:27], 0
	v_mfma_f32_16x16x32_f16 v[92:95], v[188:191], v[24:27], 0
	v_mfma_f32_16x16x32_f16 v[96:99], v[192:195], v[24:27], 0
	s_nop 1
	v_cvt_pk_f16_f32 v36, v68, v72
	s_nop 0
	v_cvt_pk_f16_f32 v37, v76, v80
	v_cvt_pk_f16_f32 v38, v69, v73
	v_cvt_pk_f16_f32 v39, v77, v81
	v_cvt_pk_f16_f32 v40, v70, v74
	v_cvt_pk_f16_f32 v41, v78, v82
	v_cvt_pk_f16_f32 v42, v71, v75
	v_cvt_pk_f16_f32 v43, v79, v83
	v_mfma_f32_16x16x32_f16 v[68:71], v[196:199], v[24:27], 0
	v_mfma_f32_16x16x32_f16 v[72:75], v[200:203], v[24:27], 0
	v_mfma_f32_16x16x32_f16 v[76:79], v[204:207], v[24:27], 0
	v_mfma_f32_16x16x32_f16 v[80:83], v[208:211], v[24:27], 0
	v_cvt_pk_f16_f32 v44, v84, v88
	v_cvt_pk_f16_f32 v45, v92, v96
	v_cvt_pk_f16_f32 v46, v85, v89
	v_cvt_pk_f16_f32 v47, v93, v97
	v_cvt_pk_f16_f32 v48, v86, v90
	v_cvt_pk_f16_f32 v49, v94, v98
	v_cvt_pk_f16_f32 v50, v87, v91
	v_cvt_pk_f16_f32 v51, v95, v99
	v_mfma_f32_16x16x32_f16 v[84:87], v[212:215], v[24:27], 0
	v_mfma_f32_16x16x32_f16 v[88:91], v[216:219], v[24:27], 0
	v_mfma_f32_16x16x32_f16 v[92:95], v[220:223], v[24:27], 0
	v_mfma_f32_16x16x32_f16 v[96:99], v[224:227], v[24:27], 0
	v_cvt_pk_f16_f32 v52, v68, v72
	v_cvt_pk_f16_f32 v53, v76, v80
	v_cvt_pk_f16_f32 v54, v69, v73
	v_cvt_pk_f16_f32 v55, v77, v81
	v_cvt_pk_f16_f32 v56, v70, v74
	v_cvt_pk_f16_f32 v57, v78, v82
	v_cvt_pk_f16_f32 v58, v71, v75
	v_cvt_pk_f16_f32 v59, v79, v83
	v_cvt_pk_f16_f32 v60, v84, v88
	v_cvt_pk_f16_f32 v61, v92, v96
	v_cvt_pk_f16_f32 v62, v85, v89
	v_cvt_pk_f16_f32 v63, v93, v97
	v_cvt_pk_f16_f32 v64, v86, v90
	v_cvt_pk_f16_f32 v65, v94, v98
	v_cvt_pk_f16_f32 v66, v87, v91
	v_cvt_pk_f16_f32 v67, v95, v99
	s_mov_b64 exec, s[38:39]
	ds_write_b128 v4, v[40:43] offset:0
	ds_write_b128 v4, v[48:51] offset:512
	ds_write_b128 v4, v[56:59] offset:1024
	ds_write_b128 v4, v[64:67] offset:1536
	s_mov_b64 exec, -1
	v_mfma_f32_16x16x32_f16 v[68:71], v[24:27], v[36:39], 0
	v_mfma_f32_16x16x32_f16 v[72:75], v[24:27], v[44:47], 0
	v_mfma_f32_16x16x32_f16 v[76:79], v[24:27], v[52:55], v[0:3]
	v_mfma_f32_16x16x32_f16 v[80:83], v[24:27], v[60:63], 0
	v_mfma_f32_16x16x32_f16 v[84:87], v[28:31], v[36:39], 0
	v_mfma_f32_16x16x32_f16 v[88:91], v[28:31], v[44:47], 0
	v_mfma_f32_16x16x32_f16 v[92:95], v[28:31], v[52:55], v[0:3]
	v_mfma_f32_16x16x32_f16 v[96:99], v[28:31], v[60:63], 0
	v_mfma_f32_16x16x32_f16 v[84:87], v[32:35], v[40:43], v[84:87]
	v_mfma_f32_16x16x32_f16 v[88:91], v[32:35], v[48:51], v[88:91]
	v_mfma_f32_16x16x32_f16 v[92:95], v[32:35], v[56:59], v[92:95]
	v_mfma_f32_16x16x32_f16 v[96:99], v[32:35], v[64:67], v[96:99]
	s_waitcnt lgkmcnt(0)
	ds_write_b32 v6, v6 offset:0
	ds_read_b32 v9, v7 offset:0
	v_mul_f32_e32 v244, v68, v72
	v_mul_f32_e32 v250, v69, v73
	v_mul_f32_e64 v245, -v72, v72
	v_mul_f32_e64 v251, -v73, v73
	v_add_f32_e32 v246, v68, v72
	v_add_f32_e32 v252, v69, v73
	v_fma_f32 v245, -v68, v68, v245
	v_fma_f32 v251, -v69, v69, v251
	v_fma_f32 v247, v10, v246, v11
	v_fma_f32 v253, v10, v252, v11
	v_fma_f32 v246, v13, v80, v14
	v_fma_f32 v252, v13, v81, v14
	v_fma_f32 v248, v12, v76, v245
	v_fma_f32 v254, v12, v77, v251
	v_fma_f32 v249, 2.0, v244, v247
	v_fma_f32 v255, 2.0, v250, v253
	v_sub_f32_e32 v247, v247, v245
	v_sub_f32_e32 v253, v253, v251
	v_fma_f32 v246, -2.0, v244, v246
	v_fma_f32 v252, -2.0, v250, v252
	v_mul_f32_e32 v247, v247, v248
	v_mul_f32_e32 v253, v253, v254
	v_rcp_f32_e32 v247, v247
	v_rcp_f32_e32 v253, v253
	v_mul_f32_e32 v249, v249, v246
	v_mul_f32_e32 v255, v255, v252
	v_fma_f32 v19, v249, v247, v19
	v_fma_f32 v19, v255, v253, v19
	v_mul_f32_e32 v244, v70, v74
	v_mul_f32_e32 v250, v71, v75
	v_mul_f32_e64 v245, -v74, v74
	v_mul_f32_e64 v251, -v75, v75
	v_add_f32_e32 v246, v70, v74
	v_add_f32_e32 v252, v71, v75
	v_fma_f32 v245, -v70, v70, v245
	v_fma_f32 v251, -v71, v71, v251
	v_fma_f32 v247, v10, v246, v11
	v_fma_f32 v253, v10, v252, v11
	v_fma_f32 v246, v13, v82, v14
	v_fma_f32 v252, v13, v83, v14
	v_fma_f32 v248, v12, v78, v245
	v_fma_f32 v254, v12, v79, v251
	v_fma_f32 v249, 2.0, v244, v247
	v_fma_f32 v255, 2.0, v250, v253
	v_sub_f32_e32 v247, v247, v245
	v_sub_f32_e32 v253, v253, v251
	v_fma_f32 v246, -2.0, v244, v246
	v_fma_f32 v252, -2.0, v250, v252
	v_mul_f32_e32 v247, v247, v248
	v_mul_f32_e32 v253, v253, v254
	v_rcp_f32_e32 v247, v247
	v_rcp_f32_e32 v253, v253
	v_mul_f32_e32 v249, v249, v246
	v_mul_f32_e32 v255, v255, v252
	v_fma_f32 v20, v249, v247, v20
	v_fma_f32 v20, v255, v253, v20
	v_mfma_f32_16x16x32_f16 v[68:71], v[24:27], v[40:43], 0
	v_mfma_f32_16x16x32_f16 v[72:75], v[24:27], v[48:51], 0
	v_mfma_f32_16x16x32_f16 v[76:79], v[24:27], v[56:59], v[0:3]
	v_mfma_f32_16x16x32_f16 v[80:83], v[24:27], v[64:67], 0
	s_barrier
	ds_read_b32 v9, v7 offset:0
	s_waitcnt lgkmcnt(0)
	v_cmp_ne_u32_e32 vcc, 0, v9
	s_cbranch_vccnz .Lq_go_0
